# same as previous best plus a 2-wait-state fix between v_cmp and v_cndmask in the gatherer fast path
# speedup vs baseline: 1.0778x; 1.0303x over previous
.LBB1_13:
	s_or_b64 exec, exec, s[2:3]
	s_mul_i32 s2, s51, s33
	v_add_u32_e32 v97, s2, v82
	v_readfirstlane_b32 s4, v0
	s_sub_i32 s4, s4, 1
	s_cmp_gt_u32 s4, 64
	s_cbranch_scc1 .Lg_slow
	s_lshl_b32 s5, s46, 11
	v_lshl_add_u32 v1, v83, 4, v87
	v_add_u32_e32 v1, s5, v1
	s_lshl_b32 s5, s46, 9
	v_lshl_add_u32 v2, v83, 2, v88
	v_add_u32_e32 v2, s5, v2
	ds_read_b128 v[8:11], v1
	ds_read_b32 v12, v2
	v_cmp_gt_u32_e64 s[6:7], s4, v83
	v_lshlrev_b32_e32 v25, 4, v69
	s_waitcnt lgkmcnt(0)
	v_cmp_neq_f32_e32 vcc, 0, v8
	s_and_b64 s[8:9], vcc, s[6:7]
	v_cmp_neq_f32_e32 vcc, 0, v9
	s_and_b64 s[10:11], vcc, s[6:7]
	v_cmp_neq_f32_e32 vcc, 0, v10
	s_and_b64 s[12:13], vcc, s[6:7]
	v_cmp_neq_f32_e32 vcc, 0, v11
	s_and_b64 s[14:15], vcc, s[6:7]
	s_bcnt1_i32_b64 s16, s[8:9]
	s_bcnt1_i32_b64 s17, s[10:11]
	s_bcnt1_i32_b64 s18, s[12:13]
	s_bcnt1_i32_b64 s19, s[14:15]
	s_add_i32 s17, s17, s16
	s_add_i32 s18, s18, s17
	s_add_i32 s19, s19, s18
	s_cmp_eq_u32 s19, 0
	s_cbranch_scc1 .Lg_slow
	s_cmp_gt_u32 s19, 64
	s_cbranch_scc1 .Lg_slow
	v_mbcnt_lo_u32_b32 v13, s8, 0
	v_mbcnt_hi_u32_b32 v13, s9, v13
	v_lshl_add_u32 v14, v13, 3, v63
	v_mov_b32_e32 v4, v12
	v_mov_b32_e32 v5, v8
	s_mov_b64 exec, s[8:9]
	ds_write_b64 v14, v[4:5]
	s_mov_b64 exec, -1
	v_mbcnt_lo_u32_b32 v13, s10, 0
	v_mbcnt_hi_u32_b32 v13, s11, v13
	v_add_u32_e32 v13, s16, v13
	v_lshl_add_u32 v14, v13, 3, v63
	v_add_u32_e32 v4, 1, v12
	v_mov_b32_e32 v5, v9
	s_mov_b64 exec, s[10:11]
	ds_write_b64 v14, v[4:5]
	s_mov_b64 exec, -1
	v_mbcnt_lo_u32_b32 v13, s12, 0
	v_mbcnt_hi_u32_b32 v13, s13, v13
	v_add_u32_e32 v13, s17, v13
	v_lshl_add_u32 v14, v13, 3, v63
	v_add_u32_e32 v4, 2, v12
	v_mov_b32_e32 v5, v10
	s_mov_b64 exec, s[12:13]
	ds_write_b64 v14, v[4:5]
	s_mov_b64 exec, -1
	v_mbcnt_lo_u32_b32 v13, s14, 0
	v_mbcnt_hi_u32_b32 v13, s15, v13
	v_add_u32_e32 v13, s18, v13
	v_lshl_add_u32 v14, v13, 3, v63
	v_add_u32_e32 v4, 3, v12
	v_mov_b32_e32 v5, v11
	s_mov_b64 exec, s[14:15]
	ds_write_b64 v14, v[4:5]
	s_mov_b64 exec, -1
	v_mov_b32_e32 v4, 0
	ds_write_b32 v6, v4
	v_cmp_gt_u32_e64 s[6:7], s19, v83
	v_lshl_add_u32 v14, v83, 3, v63
	ds_read_b64 v[16:17], v14
	v_lshl_add_u32 v22, v67, 3, v63
	ds_read_b32 v116, v22
	ds_read_b32 v117, v22 offset:32
	ds_read_b32 v118, v22 offset:64
	ds_read_b32 v119, v22 offset:96
	ds_read_b32 v120, v22 offset:128
	ds_read_b32 v121, v22 offset:160
	ds_read_b32 v122, v22 offset:192
	ds_read_b32 v123, v22 offset:224
	v_sub_u32_e32 v23, s19, v67
	s_waitcnt lgkmcnt(8)
	v_cndmask_b32_e64 v15, 0, v16, s[6:7]
	v_lshlrev_b32_e32 v15, 2, v15
	global_load_dword v18, v15, s[24:25]
	s_cmp_gt_u32 s19, 32
	s_cbranch_scc1 .Lg_big
	s_waitcnt lgkmcnt(0)
	v_cmp_lt_i32_e32 vcc, 0, v23
	v_lshl_add_u32 v24, v116, 8, v25
	s_mov_b64 exec, vcc
	global_load_dwordx4 v[136:139], v24, s[22:23]
	s_mov_b64 exec, -1
	v_cmp_lt_i32_e32 vcc, 4, v23
	v_lshl_add_u32 v24, v117, 8, v25
	s_mov_b64 exec, vcc
	global_load_dwordx4 v[140:143], v24, s[22:23]
	s_mov_b64 exec, -1
	v_cmp_lt_i32_e32 vcc, 8, v23
	v_lshl_add_u32 v24, v118, 8, v25
	s_mov_b64 exec, vcc
	global_load_dwordx4 v[144:147], v24, s[22:23]
	s_mov_b64 exec, -1
	v_cmp_lt_i32_e32 vcc, 12, v23
	v_lshl_add_u32 v24, v119, 8, v25
	s_mov_b64 exec, vcc
	global_load_dwordx4 v[148:151], v24, s[22:23]
	s_mov_b64 exec, -1
	v_cmp_lt_i32_e32 vcc, 16, v23
	v_lshl_add_u32 v24, v120, 8, v25
	s_mov_b64 exec, vcc
	global_load_dwordx4 v[152:155], v24, s[22:23]
	s_mov_b64 exec, -1
	v_cmp_lt_i32_e32 vcc, 20, v23
	v_lshl_add_u32 v24, v121, 8, v25
	s_mov_b64 exec, vcc
	global_load_dwordx4 v[156:159], v24, s[22:23]
	s_mov_b64 exec, -1
	v_cmp_lt_i32_e32 vcc, 24, v23
	v_lshl_add_u32 v24, v122, 8, v25
	s_mov_b64 exec, vcc
	global_load_dwordx4 v[160:163], v24, s[22:23]
	s_mov_b64 exec, -1
	v_cmp_lt_i32_e32 vcc, 28, v23
	v_lshl_add_u32 v24, v123, 8, v25
	s_mov_b64 exec, vcc
	global_load_dwordx4 v[164:167], v24, s[22:23]
	s_mov_b64 exec, -1
	s_waitcnt vmcnt(8)
	s_branch .Lg_soft
